# v52 + P4 unit prologue: qmax2/kmax2 loads issued with the Tsum load + P3 LayerNorm affine tail: gamma/beta kept four column tiles ahead in free registers (counted waits)
# speedup vs baseline: 1.0060x; 1.0060x over previous
.LBB0_503:
	s_or_b64 exec, exec, s[10:11]
	s_waitcnt lgkmcnt(1)
	v_and_b32_e32 v78, 0x78, v102
	v_add_u32_e32 v102, 0, v78
	v_add_u32_e32 v78, 0x20000, v102
	s_waitcnt lgkmcnt(0)
	s_barrier
	v_add_u32_e32 v80, 0x20200, v102
	ds_read_b64 v[78:79], v78
	ds_read_b64 v[80:81], v80
	v_add_u32_e32 v103, 0x20400, v102
	v_add_u32_e32 v104, 0x20600, v102
	v_add_u32_e32 v105, 0x20800, v102
	s_waitcnt lgkmcnt(1)
	v_pk_add_f32 v[78:79], v[78:79], 0 op_sel_hi:[1,0]
	v_add_u32_e32 v106, 0x20a00, v102
	s_waitcnt lgkmcnt(0)
	v_pk_add_f32 v[78:79], v[78:79], v[80:81]
	ds_read_b64 v[80:81], v103
	v_add_u32_e32 v107, 0x20c00, v102
	v_add_u32_e32 v108, 0x20e00, v102
	s_mov_b32 s18, 0x3a800000
	s_mov_b32 s14, 0xf800000
	s_waitcnt lgkmcnt(0)
	v_pk_add_f32 v[78:79], v[78:79], v[80:81]
	ds_read_b64 v[80:81], v104
	v_add_u32_e32 v110, 0x20a80, v102
	v_add_u32_e32 v111, 0x20c80, v102
	v_add_u32_e32 v112, 0x20e80, v102
	v_add_u32_e32 v113, 0x20b00, v102
	s_waitcnt lgkmcnt(0)
	v_pk_add_f32 v[78:79], v[78:79], v[80:81]
	ds_read_b64 v[80:81], v105
	v_add_u32_e32 v105, 0x20880, v102
	v_add_u32_e32 v159, 0x20d00, v102
	v_add_u32_e32 v161, 0x20f00, v102
	s_lshl_b32 s82, s3, 1
	s_waitcnt lgkmcnt(0)
	v_pk_add_f32 v[78:79], v[78:79], v[80:81]
	ds_read_b64 v[80:81], v106
	s_lshl_b32 s21, s3, 17
	s_lshl_b32 s3, s3, 11
	s_add_i32 s73, s3, 0
	s_ashr_i32 s3, s45, 31
	s_waitcnt lgkmcnt(0)
	v_pk_add_f32 v[78:79], v[78:79], v[80:81]
	ds_read_b64 v[80:81], v107
	s_lshr_b32 s3, s3, 26
	s_add_i32 s3, s45, s3
	s_ashr_i32 s3, s3, 6
	s_lshl_b32 s84, s3, 4
	s_waitcnt lgkmcnt(0)
	v_pk_add_f32 v[78:79], v[78:79], v[80:81]
	ds_read_b64 v[80:81], v108
	s_add_i32 s73, s73, 0x23000
	s_ashr_i32 s17, s16, 31
	s_ashr_i32 s85, s84, 31
	s_ashr_i32 s83, s82, 31
	s_waitcnt lgkmcnt(0)
	v_pk_add_f32 v[78:79], v[78:79], v[80:81]
	s_mov_b32 s75, 0
	v_pk_mul_f32 v[106:107], v[78:79], s[18:19] op_sel_hi:[1,0]
	s_nop 0
	v_fma_f32 v78, -v106, v106, v107
	v_max_f32_e32 v78, 0, v78
	v_add_f32_e32 v78, 0x3727c5ac, v78
	v_cmp_gt_f32_e32 vcc, s14, v78
	v_mul_f32_e32 v79, 0x4f800000, v78
	v_pk_add_f32 v[46:47], v[46:47], v[106:107] op_sel_hi:[1,0] neg_lo:[0,1] neg_hi:[0,1]
	v_cndmask_b32_e32 v78, v78, v79, vcc
	v_sqrt_f32_e32 v79, v78
	v_pk_add_f32 v[48:49], v[48:49], v[106:107] op_sel_hi:[1,0] neg_lo:[0,1] neg_hi:[0,1]
	v_pk_add_f32 v[34:35], v[34:35], v[106:107] op_sel_hi:[1,0] neg_lo:[0,1] neg_hi:[0,1]
	v_pk_add_f32 v[36:37], v[36:37], v[106:107] op_sel_hi:[1,0] neg_lo:[0,1] neg_hi:[0,1]
	v_add_u32_e32 v80, -1, v79
	v_fma_f32 v81, -v80, v79, v78
	v_cmp_ge_f32_e64 s[10:11], 0, v81
	v_add_u32_e32 v81, 1, v79
	v_pk_add_f32 v[26:27], v[26:27], v[106:107] op_sel_hi:[1,0] neg_lo:[0,1] neg_hi:[0,1]
	v_cndmask_b32_e64 v80, v79, v80, s[10:11]
	v_fma_f32 v79, -v81, v79, v78
	v_cmp_lt_f32_e64 s[10:11], 0, v79
	v_pk_add_f32 v[28:29], v[28:29], v[106:107] op_sel_hi:[1,0] neg_lo:[0,1] neg_hi:[0,1]
	v_pk_add_f32 v[42:43], v[42:43], v[106:107] op_sel_hi:[1,0] neg_lo:[0,1] neg_hi:[0,1]
	v_cndmask_b32_e64 v79, v80, v81, s[10:11]
	v_mul_f32_e32 v80, 0x37800000, v79
	v_cndmask_b32_e32 v79, v79, v80, vcc
	v_cmp_class_f32_e32 vcc, v78, v224
	v_pk_add_f32 v[44:45], v[44:45], v[106:107] op_sel_hi:[1,0] neg_lo:[0,1] neg_hi:[0,1]
	v_pk_add_f32 v[30:31], v[30:31], v[106:107] op_sel_hi:[1,0] neg_lo:[0,1] neg_hi:[0,1]
	v_cndmask_b32_e32 v78, v79, v78, vcc
	v_div_scale_f32 v79, s[10:11], v78, v78, 1.0
	v_rcp_f32_e32 v80, v79
	v_pk_add_f32 v[32:33], v[32:33], v[106:107] op_sel_hi:[1,0] neg_lo:[0,1] neg_hi:[0,1]
	v_pk_add_f32 v[22:23], v[22:23], v[106:107] op_sel_hi:[1,0] neg_lo:[0,1] neg_hi:[0,1]
	v_pk_add_f32 v[24:25], v[24:25], v[106:107] op_sel_hi:[1,0] neg_lo:[0,1] neg_hi:[0,1]
	v_fma_f32 v81, -v79, v80, 1.0
	v_fmac_f32_e32 v80, v81, v80
	v_div_scale_f32 v81, vcc, 1.0, v78, 1.0
	v_mul_f32_e32 v103, v81, v80
	v_fma_f32 v104, -v79, v103, v81
	v_fmac_f32_e32 v103, v104, v80
	v_fma_f32 v79, -v79, v103, v81
	v_div_fmas_f32 v79, v79, v80, v103
	v_div_fixup_f32 v108, v79, v78, 1.0
	v_add_u32_e32 v78, 0x20080, v102
	v_add_u32_e32 v80, 0x20280, v102
	ds_read_b64 v[78:79], v78
	ds_read_b64 v[80:81], v80
	v_add_u32_e32 v103, 0x20480, v102
	v_add_u32_e32 v104, 0x20680, v102
	v_pk_mul_f32 v[46:47], v[46:47], v[108:109] op_sel_hi:[1,0]
	s_waitcnt lgkmcnt(1)
	v_pk_add_f32 v[78:79], v[78:79], 0 op_sel_hi:[1,0]
	v_pk_mul_f32 v[48:49], v[48:49], v[108:109] op_sel_hi:[1,0]
	s_waitcnt lgkmcnt(0)
	v_pk_add_f32 v[78:79], v[78:79], v[80:81]
	ds_read_b64 v[80:81], v103
	v_pk_mul_f32 v[34:35], v[34:35], v[108:109] op_sel_hi:[1,0]
	v_pk_mul_f32 v[36:37], v[36:37], v[108:109] op_sel_hi:[1,0]
	v_pk_mul_f32 v[26:27], v[26:27], v[108:109] op_sel_hi:[1,0]
	v_pk_mul_f32 v[28:29], v[28:29], v[108:109] op_sel_hi:[1,0]
	s_waitcnt lgkmcnt(0)
	v_pk_add_f32 v[78:79], v[78:79], v[80:81]
	ds_read_b64 v[80:81], v104
	v_pk_mul_f32 v[42:43], v[42:43], v[108:109] op_sel_hi:[1,0]
	v_pk_mul_f32 v[44:45], v[44:45], v[108:109] op_sel_hi:[1,0]
	v_pk_mul_f32 v[30:31], v[30:31], v[108:109] op_sel_hi:[1,0]
	v_pk_mul_f32 v[32:33], v[32:33], v[108:109] op_sel_hi:[1,0]
	s_waitcnt lgkmcnt(0)
	v_pk_add_f32 v[78:79], v[78:79], v[80:81]
	ds_read_b64 v[80:81], v105
	v_add_u32_e32 v105, 0x20900, v102
	v_pk_mul_f32 v[22:23], v[22:23], v[108:109] op_sel_hi:[1,0]
	v_pk_mul_f32 v[24:25], v[24:25], v[108:109] op_sel_hi:[1,0]
	v_pk_add_f32 v[6:7], v[6:7], v[106:107] op_sel_hi:[1,0] neg_lo:[0,1] neg_hi:[0,1]
	s_waitcnt lgkmcnt(0)
	v_pk_add_f32 v[78:79], v[78:79], v[80:81]
	ds_read_b64 v[80:81], v110
	v_pk_add_f32 v[8:9], v[8:9], v[106:107] op_sel_hi:[1,0] neg_lo:[0,1] neg_hi:[0,1]
	v_pk_mul_f32 v[6:7], v[6:7], v[108:109] op_sel_hi:[1,0]
	v_pk_mul_f32 v[8:9], v[8:9], v[108:109] op_sel_hi:[1,0]
	v_pk_add_f32 v[2:3], v[2:3], v[106:107] op_sel_hi:[1,0] neg_lo:[0,1] neg_hi:[0,1]
	s_waitcnt lgkmcnt(0)
	v_pk_add_f32 v[78:79], v[78:79], v[80:81]
	ds_read_b64 v[80:81], v111
	v_pk_add_f32 v[4:5], v[4:5], v[106:107] op_sel_hi:[1,0] neg_lo:[0,1] neg_hi:[0,1]
	v_pk_mul_f32 v[2:3], v[2:3], v[108:109] op_sel_hi:[1,0]
	v_pk_mul_f32 v[4:5], v[4:5], v[108:109] op_sel_hi:[1,0]
	s_waitcnt lgkmcnt(0)
	v_pk_add_f32 v[78:79], v[78:79], v[80:81]
	ds_read_b64 v[80:81], v112
	s_waitcnt lgkmcnt(0)
	v_pk_add_f32 v[78:79], v[78:79], v[80:81]
	s_nop 0
	v_pk_mul_f32 v[110:111], v[78:79], s[18:19] op_sel_hi:[1,0]
	s_nop 0
	v_fma_f32 v78, -v110, v110, v111
	v_max_f32_e32 v78, 0, v78
	v_add_f32_e32 v78, 0x3727c5ac, v78
	v_cmp_gt_f32_e32 vcc, s14, v78
	v_mul_f32_e32 v79, 0x4f800000, v78
	s_nop 0
	v_cndmask_b32_e32 v78, v78, v79, vcc
	v_sqrt_f32_e32 v79, v78
	s_nop 0
	v_add_u32_e32 v80, -1, v79
	v_fma_f32 v81, -v80, v79, v78
	v_cmp_ge_f32_e64 s[10:11], 0, v81
	v_add_u32_e32 v81, 1, v79
	s_nop 0
	v_cndmask_b32_e64 v80, v79, v80, s[10:11]
	v_fma_f32 v79, -v81, v79, v78
	v_cmp_lt_f32_e64 s[10:11], 0, v79
	s_nop 1
	v_cndmask_b32_e64 v79, v80, v81, s[10:11]
	v_mul_f32_e32 v80, 0x37800000, v79
	v_cndmask_b32_e32 v79, v79, v80, vcc
	v_cmp_class_f32_e32 vcc, v78, v224
	s_nop 1
	v_cndmask_b32_e32 v78, v79, v78, vcc
	v_div_scale_f32 v79, s[10:11], v78, v78, 1.0
	v_rcp_f32_e32 v80, v79
	s_nop 0
	v_fma_f32 v81, -v79, v80, 1.0
	v_fmac_f32_e32 v80, v81, v80
	v_div_scale_f32 v81, vcc, 1.0, v78, 1.0
	v_mul_f32_e32 v103, v81, v80
	v_fma_f32 v104, -v79, v103, v81
	v_fmac_f32_e32 v103, v104, v80
	v_fma_f32 v79, -v79, v103, v81
	v_div_fmas_f32 v79, v79, v80, v103
	v_div_fixup_f32 v112, v79, v78, 1.0
	v_add_u32_e32 v78, 0x20100, v102
	v_add_u32_e32 v80, 0x20300, v102
	ds_read_b64 v[78:79], v78
	ds_read_b64 v[80:81], v80
	v_add_u32_e32 v103, 0x20500, v102
	v_add_u32_e32 v104, 0x20700, v102
	s_waitcnt lgkmcnt(1)
	v_pk_add_f32 v[78:79], v[78:79], 0 op_sel_hi:[1,0]
	s_waitcnt lgkmcnt(0)
	v_pk_add_f32 v[78:79], v[78:79], v[80:81]
	ds_read_b64 v[80:81], v103
	s_waitcnt lgkmcnt(0)
	v_pk_add_f32 v[78:79], v[78:79], v[80:81]
	ds_read_b64 v[80:81], v104
	s_waitcnt lgkmcnt(0)
	v_pk_add_f32 v[78:79], v[78:79], v[80:81]
	ds_read_b64 v[80:81], v105
	v_add_u32_e32 v105, 0x20980, v102
	s_waitcnt lgkmcnt(0)
	v_pk_add_f32 v[78:79], v[78:79], v[80:81]
	ds_read_b64 v[80:81], v113
	v_add_u32_e32 v113, 0x20b80, v102
	s_waitcnt lgkmcnt(0)
	v_pk_add_f32 v[78:79], v[78:79], v[80:81]
	ds_read_b64 v[80:81], v159
	v_add_u32_e32 v159, 0x20d80, v102
	s_waitcnt lgkmcnt(0)
	v_pk_add_f32 v[78:79], v[78:79], v[80:81]
	ds_read_b64 v[80:81], v161
	v_ashrrev_i32_e32 v161, 31, v160
	s_waitcnt lgkmcnt(0)
	v_pk_add_f32 v[78:79], v[78:79], v[80:81]
	s_nop 0
	v_pk_mul_f32 v[166:167], v[78:79], s[18:19] op_sel_hi:[1,0]
	s_nop 0
	v_fma_f32 v78, -v166, v166, v167
	v_max_f32_e32 v78, 0, v78
	v_add_f32_e32 v78, 0x3727c5ac, v78
	v_cmp_gt_f32_e32 vcc, s14, v78
	v_mul_f32_e32 v79, 0x4f800000, v78
	s_nop 0
	v_cndmask_b32_e32 v78, v78, v79, vcc
	v_sqrt_f32_e32 v79, v78
	s_nop 0
	v_add_u32_e32 v80, -1, v79
	v_fma_f32 v81, -v80, v79, v78
	v_cmp_ge_f32_e64 s[10:11], 0, v81
	v_add_u32_e32 v81, 1, v79
	s_nop 0
	v_cndmask_b32_e64 v80, v79, v80, s[10:11]
	v_fma_f32 v79, -v81, v79, v78
	v_cmp_lt_f32_e64 s[10:11], 0, v79
	s_nop 1
	v_cndmask_b32_e64 v79, v80, v81, s[10:11]
	v_mul_f32_e32 v80, 0x37800000, v79
	v_cndmask_b32_e32 v79, v79, v80, vcc
	v_cmp_class_f32_e32 vcc, v78, v224
	s_nop 1
	v_cndmask_b32_e32 v78, v79, v78, vcc
	v_div_scale_f32 v79, s[10:11], v78, v78, 1.0
	v_rcp_f32_e32 v80, v79
	s_nop 0
	v_fma_f32 v81, -v79, v80, 1.0
	v_fmac_f32_e32 v80, v81, v80
	v_div_scale_f32 v81, vcc, 1.0, v78, 1.0
	v_mul_f32_e32 v103, v81, v80
	v_fma_f32 v104, -v79, v103, v81
	v_fmac_f32_e32 v103, v104, v80
	v_fma_f32 v79, -v79, v103, v81
	v_div_fmas_f32 v79, v79, v80, v103
	v_div_fixup_f32 v168, v79, v78, 1.0
	v_add_u32_e32 v78, 0x20180, v102
	v_add_u32_e32 v80, 0x20380, v102
	ds_read_b64 v[78:79], v78
	ds_read_b64 v[80:81], v80
	v_add_u32_e32 v103, 0x20580, v102
	v_add_u32_e32 v104, 0x20780, v102
	v_add_u32_e32 v102, 0x20f80, v102
	s_waitcnt lgkmcnt(1)
	v_pk_add_f32 v[78:79], v[78:79], 0 op_sel_hi:[1,0]
	s_waitcnt lgkmcnt(0)
	v_pk_add_f32 v[78:79], v[78:79], v[80:81]
	ds_read_b64 v[80:81], v103
	s_waitcnt lgkmcnt(0)
	v_pk_add_f32 v[78:79], v[78:79], v[80:81]
	ds_read_b64 v[80:81], v104
	s_waitcnt lgkmcnt(0)
	v_pk_add_f32 v[78:79], v[78:79], v[80:81]
	ds_read_b64 v[80:81], v105
	s_waitcnt lgkmcnt(0)
	v_pk_add_f32 v[78:79], v[78:79], v[80:81]
	ds_read_b64 v[80:81], v113
	s_waitcnt lgkmcnt(0)
	v_pk_add_f32 v[78:79], v[78:79], v[80:81]
	ds_read_b64 v[80:81], v159
	v_ashrrev_i32_e32 v159, 31, v158
	s_waitcnt lgkmcnt(0)
	v_pk_add_f32 v[78:79], v[78:79], v[80:81]
	ds_read_b64 v[80:81], v102
	s_waitcnt lgkmcnt(0)
	v_pk_add_f32 v[78:79], v[78:79], v[80:81]
	s_nop 0
	v_pk_mul_f32 v[162:163], v[78:79], s[18:19] op_sel_hi:[1,0]
	v_readlane_b32 s18, v255, 5
	v_fma_f32 v78, -v162, v162, v163
	v_max_f32_e32 v78, 0, v78
	v_add_f32_e32 v78, 0x3727c5ac, v78
	v_cmp_gt_f32_e32 vcc, s14, v78
	v_mul_f32_e32 v79, 0x4f800000, v78
	v_readlane_b32 s19, v255, 6
	v_cndmask_b32_e32 v78, v78, v79, vcc
	v_sqrt_f32_e32 v79, v78
	v_readlane_b32 s14, v254, 19
	v_readlane_b32 s15, v254, 20
	v_add_u32_e32 v80, -1, v79
	v_fma_f32 v81, -v80, v79, v78
	v_cmp_ge_f32_e64 s[10:11], 0, v81
	v_add_u32_e32 v81, 1, v79
	s_nop 0
	v_cndmask_b32_e64 v80, v79, v80, s[10:11]
	v_fma_f32 v79, -v81, v79, v78
	v_cmp_lt_f32_e64 s[10:11], 0, v79
	s_nop 1
	v_cndmask_b32_e64 v79, v80, v81, s[10:11]
	v_mul_f32_e32 v80, 0x37800000, v79
	v_cndmask_b32_e32 v79, v79, v80, vcc
	v_cmp_class_f32_e32 vcc, v78, v224
	s_nop 1
	v_cndmask_b32_e32 v78, v79, v78, vcc
	v_div_scale_f32 v79, s[10:11], v78, v78, 1.0
	v_rcp_f32_e32 v80, v79
	v_readlane_b32 s10, v255, 3
	v_readlane_b32 s11, v255, 4
	v_writelane_b32 v255, s45, 26
	v_fma_f32 v81, -v79, v80, 1.0
	v_fmac_f32_e32 v80, v81, v80
	v_div_scale_f32 v81, vcc, 1.0, v78, 1.0
	v_mul_f32_e32 v102, v81, v80
	v_fma_f32 v103, -v79, v102, v81
	v_fmac_f32_e32 v102, v103, v80
	v_fma_f32 v79, -v79, v102, v81
	v_div_fmas_f32 v79, v79, v80, v102
	v_div_fixup_f32 v164, v79, v78, 1.0
	v_lshlrev_b32_e32 v170, 2, v160
	v_lshlrev_b32_e32 v174, 2, v160
	global_load_dwordx4 v[170:173], v170, s[10:11]
	global_load_dwordx4 v[174:177], v174, s[18:19]
	v_lshlrev_b32_e32 v178, 2, v158
	v_lshlrev_b32_e32 v182, 2, v158
	global_load_dwordx4 v[178:181], v178, s[10:11]
	global_load_dwordx4 v[182:185], v182, s[18:19]
	v_lshlrev_b32_e32 v186, 2, v154
	v_lshlrev_b32_e32 v190, 2, v154
	global_load_dwordx4 v[186:189], v186, s[10:11]
	global_load_dwordx4 v[190:193], v190, s[18:19]
	v_lshlrev_b32_e32 v194, 2, v152
	v_lshlrev_b32_e32 v198, 2, v152
	global_load_dwordx4 v[194:197], v194, s[10:11]
	global_load_dwordx4 v[198:201], v198, s[18:19]
	v_lshlrev_b64 v[78:79], 2, v[160:161]
	v_lshl_add_u64 v[80:81], s[10:11], 0, v[78:79]
	v_lshl_add_u64 v[102:103], s[18:19], 0, v[78:79]
	s_nop 0
	s_waitcnt vmcnt(6)
	v_pk_fma_f32 v[46:47], v[46:47], v[170:171], v[174:175]
	v_pk_fma_f32 v[48:49], v[48:49], v[172:173], v[176:177]
	v_cvt_pk_bf16_f32 v46, v46, v47
	v_cvt_pk_bf16_f32 v47, v48, v49
	v_pk_add_f32 v[48:49], v[94:95], v[110:111] op_sel_hi:[1,0] neg_lo:[0,1] neg_hi:[0,1]
	v_pk_add_f32 v[94:95], v[96:97], v[110:111] op_sel_hi:[1,0] neg_lo:[0,1] neg_hi:[0,1]
	v_pk_mul_f32 v[48:49], v[48:49], v[112:113] op_sel_hi:[1,0]
	v_pk_mul_f32 v[94:95], v[94:95], v[112:113] op_sel_hi:[1,0]
	v_pk_fma_f32 v[48:49], v[48:49], v[170:171], v[174:175]
	v_pk_fma_f32 v[94:95], v[94:95], v[172:173], v[176:177]
	v_cvt_pk_bf16_f32 v48, v48, v49
	v_cvt_pk_bf16_f32 v49, v94, v95
	ds_write2st64_b64 v157, v[46:47], v[48:49] offset1:64
	v_pk_add_f32 v[46:47], v[126:127], v[166:167] op_sel_hi:[1,0] neg_lo:[0,1] neg_hi:[0,1]
	v_pk_add_f32 v[48:49], v[128:129], v[166:167] op_sel_hi:[1,0] neg_lo:[0,1] neg_hi:[0,1]
	v_pk_mul_f32 v[46:47], v[46:47], v[168:169] op_sel_hi:[1,0]
	v_pk_mul_f32 v[48:49], v[48:49], v[168:169] op_sel_hi:[1,0]
	v_pk_fma_f32 v[46:47], v[46:47], v[170:171], v[174:175]
	v_pk_fma_f32 v[48:49], v[48:49], v[172:173], v[176:177]
	v_cvt_pk_bf16_f32 v46, v46, v47
	v_cvt_pk_bf16_f32 v47, v48, v49
	v_add_u32_e32 v48, 0x10000, v157
	ds_write_b64 v48, v[46:47]
	v_pk_add_f32 v[46:47], v[142:143], v[162:163] op_sel_hi:[1,0] neg_lo:[0,1] neg_hi:[0,1]
	v_pk_add_f32 v[48:49], v[144:145], v[162:163] op_sel_hi:[1,0] neg_lo:[0,1] neg_hi:[0,1]
	v_pk_mul_f32 v[46:47], v[46:47], v[164:165] op_sel_hi:[1,0]
	v_pk_mul_f32 v[48:49], v[48:49], v[164:165] op_sel_hi:[1,0]
	v_pk_fma_f32 v[46:47], v[170:171], v[46:47], v[174:175]
	v_pk_fma_f32 v[48:49], v[172:173], v[48:49], v[176:177]
	v_lshlrev_b32_e32 v170, 2, v156
	v_lshlrev_b32_e32 v174, 2, v156
	global_load_dwordx4 v[170:173], v170, s[10:11]
	global_load_dwordx4 v[174:177], v174, s[18:19]
	v_cvt_pk_bf16_f32 v46, v46, v47
	v_cvt_pk_bf16_f32 v47, v48, v49
	v_add_u32_e32 v48, 0x18000, v157
	ds_write_b64 v48, v[46:47]
	v_lshlrev_b64 v[46:47], 2, v[158:159]
	v_lshl_add_u64 v[48:49], s[10:11], 0, v[46:47]
	v_lshl_add_u64 v[78:79], s[18:19], 0, v[46:47]
	s_nop 0
	v_ashrrev_i32_e32 v157, 31, v156
	s_waitcnt vmcnt(6)
	v_pk_fma_f32 v[34:35], v[34:35], v[178:179], v[182:183]
	v_pk_fma_f32 v[36:37], v[36:37], v[180:181], v[184:185]
	v_cvt_pk_bf16_f32 v34, v34, v35
	v_cvt_pk_bf16_f32 v35, v36, v37
	v_pk_add_f32 v[36:37], v[82:83], v[110:111] op_sel_hi:[1,0] neg_lo:[0,1] neg_hi:[0,1]
	v_pk_add_f32 v[82:83], v[84:85], v[110:111] op_sel_hi:[1,0] neg_lo:[0,1] neg_hi:[0,1]
	v_pk_mul_f32 v[36:37], v[36:37], v[112:113] op_sel_hi:[1,0]
	v_pk_mul_f32 v[82:83], v[82:83], v[112:113] op_sel_hi:[1,0]
	v_pk_fma_f32 v[36:37], v[36:37], v[178:179], v[182:183]
	v_pk_fma_f32 v[82:83], v[82:83], v[180:181], v[184:185]
	v_cvt_pk_bf16_f32 v36, v36, v37
	v_cvt_pk_bf16_f32 v37, v82, v83
	ds_write2st64_b64 v155, v[34:35], v[36:37] offset1:64
	v_pk_add_f32 v[34:35], v[118:119], v[166:167] op_sel_hi:[1,0] neg_lo:[0,1] neg_hi:[0,1]
	v_pk_add_f32 v[36:37], v[120:121], v[166:167] op_sel_hi:[1,0] neg_lo:[0,1] neg_hi:[0,1]
	v_pk_mul_f32 v[34:35], v[34:35], v[168:169] op_sel_hi:[1,0]
	v_pk_mul_f32 v[36:37], v[36:37], v[168:169] op_sel_hi:[1,0]
	v_pk_fma_f32 v[34:35], v[34:35], v[178:179], v[182:183]
	v_pk_fma_f32 v[36:37], v[36:37], v[180:181], v[184:185]
	v_cvt_pk_bf16_f32 v34, v34, v35
	v_cvt_pk_bf16_f32 v35, v36, v37
	v_add_u32_e32 v36, 0x10000, v155
	ds_write_b64 v36, v[34:35]
	v_pk_add_f32 v[34:35], v[134:135], v[162:163] op_sel_hi:[1,0] neg_lo:[0,1] neg_hi:[0,1]
	v_pk_add_f32 v[36:37], v[136:137], v[162:163] op_sel_hi:[1,0] neg_lo:[0,1] neg_hi:[0,1]
	v_pk_mul_f32 v[34:35], v[34:35], v[164:165] op_sel_hi:[1,0]
	v_pk_mul_f32 v[36:37], v[36:37], v[164:165] op_sel_hi:[1,0]
	v_pk_fma_f32 v[34:35], v[34:35], v[178:179], v[182:183]
	v_pk_fma_f32 v[36:37], v[36:37], v[180:181], v[184:185]
	v_lshlrev_b32_e32 v178, 2, v150
	v_lshlrev_b32_e32 v182, 2, v150
	global_load_dwordx4 v[178:181], v178, s[10:11]
	global_load_dwordx4 v[182:185], v182, s[18:19]
	v_cvt_pk_bf16_f32 v34, v34, v35
	v_cvt_pk_bf16_f32 v35, v36, v37
	v_add_u32_e32 v36, 0x18000, v155
	v_ashrrev_i32_e32 v155, 31, v154
	ds_write_b64 v36, v[34:35]
	v_lshlrev_b64 v[34:35], 2, v[154:155]
	v_lshl_add_u64 v[36:37], s[10:11], 0, v[34:35]
	v_lshl_add_u64 v[46:47], s[18:19], 0, v[34:35]
	s_nop 0
	s_waitcnt vmcnt(6)
	v_pk_fma_f32 v[26:27], v[26:27], v[186:187], v[190:191]
	v_pk_fma_f32 v[28:29], v[28:29], v[188:189], v[192:193]
	v_cvt_pk_bf16_f32 v26, v26, v27
	v_cvt_pk_bf16_f32 v27, v28, v29
	v_pk_add_f32 v[28:29], v[74:75], v[110:111] op_sel_hi:[1,0] neg_lo:[0,1] neg_hi:[0,1]
	v_pk_add_f32 v[74:75], v[76:77], v[110:111] op_sel_hi:[1,0] neg_lo:[0,1] neg_hi:[0,1]
	v_pk_mul_f32 v[28:29], v[28:29], v[112:113] op_sel_hi:[1,0]
	v_pk_mul_f32 v[74:75], v[74:75], v[112:113] op_sel_hi:[1,0]
	v_pk_fma_f32 v[28:29], v[28:29], v[186:187], v[190:191]
	v_pk_fma_f32 v[74:75], v[74:75], v[188:189], v[192:193]
	v_cvt_pk_bf16_f32 v28, v28, v29
	v_cvt_pk_bf16_f32 v29, v74, v75
	ds_write2st64_b64 v153, v[26:27], v[28:29] offset1:64
	v_pk_add_f32 v[26:27], v[114:115], v[166:167] op_sel_hi:[1,0] neg_lo:[0,1] neg_hi:[0,1]
	v_pk_add_f32 v[28:29], v[116:117], v[166:167] op_sel_hi:[1,0] neg_lo:[0,1] neg_hi:[0,1]
	v_pk_mul_f32 v[26:27], v[26:27], v[168:169] op_sel_hi:[1,0]
	v_pk_mul_f32 v[28:29], v[28:29], v[168:169] op_sel_hi:[1,0]
	v_pk_fma_f32 v[26:27], v[26:27], v[186:187], v[190:191]
	v_pk_fma_f32 v[28:29], v[28:29], v[188:189], v[192:193]
	v_cvt_pk_bf16_f32 v26, v26, v27
	v_cvt_pk_bf16_f32 v27, v28, v29
	v_add_u32_e32 v28, 0x10000, v153
	ds_write_b64 v28, v[26:27]
	v_pk_add_f32 v[26:27], v[130:131], v[162:163] op_sel_hi:[1,0] neg_lo:[0,1] neg_hi:[0,1]
	v_pk_add_f32 v[28:29], v[132:133], v[162:163] op_sel_hi:[1,0] neg_lo:[0,1] neg_hi:[0,1]
	v_pk_mul_f32 v[26:27], v[26:27], v[164:165] op_sel_hi:[1,0]
	v_pk_mul_f32 v[28:29], v[28:29], v[164:165] op_sel_hi:[1,0]
	v_pk_fma_f32 v[26:27], v[26:27], v[186:187], v[190:191]
	v_pk_fma_f32 v[28:29], v[28:29], v[188:189], v[192:193]
	v_lshlrev_b32_e32 v186, 2, v148
	v_lshlrev_b32_e32 v190, 2, v148
	global_load_dwordx4 v[186:189], v186, s[10:11]
	global_load_dwordx4 v[190:193], v190, s[18:19]
	v_cvt_pk_bf16_f32 v26, v26, v27
	v_cvt_pk_bf16_f32 v27, v28, v29
	v_add_u32_e32 v28, 0x18000, v153
	v_ashrrev_i32_e32 v153, 31, v152
	ds_write_b64 v28, v[26:27]
	v_lshlrev_b64 v[26:27], 2, v[152:153]
	v_lshl_add_u64 v[28:29], s[10:11], 0, v[26:27]
	v_lshl_add_u64 v[34:35], s[18:19], 0, v[26:27]
	s_nop 0
	v_pk_add_f32 v[46:47], v[88:89], v[110:111] op_sel_hi:[1,0] neg_lo:[0,1] neg_hi:[0,1]
	s_waitcnt vmcnt(6)
	v_pk_fma_f32 v[42:43], v[42:43], v[194:195], v[198:199]
	v_pk_fma_f32 v[44:45], v[44:45], v[196:197], v[200:201]
	v_cvt_pk_bf16_f32 v42, v42, v43
	v_cvt_pk_bf16_f32 v43, v44, v45
	v_pk_add_f32 v[44:45], v[86:87], v[110:111] op_sel_hi:[1,0] neg_lo:[0,1] neg_hi:[0,1]
	v_pk_mul_f32 v[46:47], v[46:47], v[112:113] op_sel_hi:[1,0]
	v_pk_mul_f32 v[44:45], v[44:45], v[112:113] op_sel_hi:[1,0]
	v_pk_fma_f32 v[46:47], v[46:47], v[196:197], v[200:201]
	v_pk_fma_f32 v[44:45], v[44:45], v[194:195], v[198:199]
	s_nop 0
	v_cvt_pk_bf16_f32 v44, v44, v45
	v_cvt_pk_bf16_f32 v45, v46, v47
	ds_write2st64_b64 v151, v[42:43], v[44:45] offset1:64
	v_pk_add_f32 v[42:43], v[122:123], v[166:167] op_sel_hi:[1,0] neg_lo:[0,1] neg_hi:[0,1]
	v_pk_add_f32 v[44:45], v[124:125], v[166:167] op_sel_hi:[1,0] neg_lo:[0,1] neg_hi:[0,1]
	v_pk_mul_f32 v[42:43], v[42:43], v[168:169] op_sel_hi:[1,0]
	v_pk_mul_f32 v[44:45], v[44:45], v[168:169] op_sel_hi:[1,0]
	v_pk_fma_f32 v[42:43], v[42:43], v[194:195], v[198:199]
	v_pk_fma_f32 v[44:45], v[44:45], v[196:197], v[200:201]
	v_cvt_pk_bf16_f32 v42, v42, v43
	v_cvt_pk_bf16_f32 v43, v44, v45
	v_add_u32_e32 v44, 0x10000, v151
	ds_write_b64 v44, v[42:43]
	v_pk_add_f32 v[42:43], v[138:139], v[162:163] op_sel_hi:[1,0] neg_lo:[0,1] neg_hi:[0,1]
	s_nop 0
	v_pk_mul_f32 v[42:43], v[42:43], v[164:165] op_sel_hi:[1,0]
	s_nop 0
	v_pk_fma_f32 v[26:27], v[42:43], v[194:195], v[198:199]
	v_pk_add_f32 v[34:35], v[140:141], v[162:163] op_sel_hi:[1,0] neg_lo:[0,1] neg_hi:[0,1]
	v_cvt_pk_bf16_f32 v26, v26, v27
	v_pk_mul_f32 v[34:35], v[34:35], v[164:165] op_sel_hi:[1,0]
	v_pk_add_f32 v[42:43], v[72:73], v[110:111] op_sel_hi:[1,0] neg_lo:[0,1] neg_hi:[0,1]
	v_pk_fma_f32 v[28:29], v[34:35], v[196:197], v[200:201]
	v_lshlrev_b32_e32 v194, 2, v146
	v_lshlrev_b32_e32 v198, 2, v146
	global_load_dwordx4 v[194:197], v194, s[10:11]
	global_load_dwordx4 v[198:201], v198, s[18:19]
	v_pk_mul_f32 v[42:43], v[42:43], v[112:113] op_sel_hi:[1,0]
	v_cvt_pk_bf16_f32 v27, v28, v29
	v_add_u32_e32 v28, 0x18000, v151
	ds_write_b64 v28, v[26:27]
	v_lshlrev_b64 v[26:27], 2, v[156:157]
	v_lshl_add_u64 v[28:29], s[10:11], 0, v[26:27]
	v_lshl_add_u64 v[34:35], s[18:19], 0, v[26:27]
	s_nop 0
	v_ashrrev_i32_e32 v151, 31, v150
	s_waitcnt vmcnt(6)
	v_pk_fma_f32 v[30:31], v[30:31], v[170:171], v[174:175]
	v_pk_fma_f32 v[32:33], v[32:33], v[172:173], v[176:177]
	v_cvt_pk_bf16_f32 v30, v30, v31
	v_cvt_pk_bf16_f32 v31, v32, v33
	v_pk_add_f32 v[32:33], v[70:71], v[110:111] op_sel_hi:[1,0] neg_lo:[0,1] neg_hi:[0,1]
	v_pk_fma_f32 v[42:43], v[42:43], v[172:173], v[176:177]
	v_pk_mul_f32 v[32:33], v[32:33], v[112:113] op_sel_hi:[1,0]
	s_nop 0
	v_pk_fma_f32 v[32:33], v[32:33], v[170:171], v[174:175]
	s_nop 0
	v_cvt_pk_bf16_f32 v32, v32, v33
	v_cvt_pk_bf16_f32 v33, v42, v43
	ds_write2st64_b64 v169, v[30:31], v[32:33] offset1:64
	v_pk_add_f32 v[30:31], v[98:99], v[166:167] op_sel_hi:[1,0] neg_lo:[0,1] neg_hi:[0,1]
	v_pk_add_f32 v[32:33], v[100:101], v[166:167] op_sel_hi:[1,0] neg_lo:[0,1] neg_hi:[0,1]
	v_pk_mul_f32 v[30:31], v[30:31], v[168:169] op_sel_hi:[1,0]
	v_pk_mul_f32 v[32:33], v[32:33], v[168:169] op_sel_hi:[1,0]
	v_pk_fma_f32 v[30:31], v[30:31], v[170:171], v[174:175]
	v_pk_fma_f32 v[32:33], v[32:33], v[172:173], v[176:177]
	v_cvt_pk_bf16_f32 v30, v30, v31
	v_cvt_pk_bf16_f32 v31, v32, v33
	v_add_u32_e32 v32, 0x10000, v169
	ds_write_b64 v32, v[30:31]
	v_pk_add_f32 v[30:31], v[50:51], v[162:163] op_sel_hi:[1,0] neg_lo:[0,1] neg_hi:[0,1]
	s_nop 0
	v_pk_mul_f32 v[30:31], v[30:31], v[164:165] op_sel_hi:[1,0]
	s_nop 0
	v_pk_fma_f32 v[26:27], v[30:31], v[170:171], v[174:175]
	v_pk_add_f32 v[30:31], v[52:53], v[162:163] op_sel_hi:[1,0] neg_lo:[0,1] neg_hi:[0,1]
	v_cvt_pk_bf16_f32 v26, v26, v27
	v_pk_mul_f32 v[30:31], v[30:31], v[164:165] op_sel_hi:[1,0]
	v_pk_add_f32 v[34:35], v[64:65], v[110:111] op_sel_hi:[1,0] neg_lo:[0,1] neg_hi:[0,1]
	v_pk_fma_f32 v[28:29], v[30:31], v[172:173], v[176:177]
	v_pk_mul_f32 v[34:35], v[34:35], v[112:113] op_sel_hi:[1,0]
	v_cvt_pk_bf16_f32 v27, v28, v29
	v_add_u32_e32 v28, 0x18000, v169
	ds_write_b64 v28, v[26:27]
	v_lshlrev_b64 v[26:27], 2, v[150:151]
	v_lshl_add_u64 v[28:29], s[10:11], 0, v[26:27]
	v_lshl_add_u64 v[30:31], s[18:19], 0, v[26:27]
	s_nop 0
	s_waitcnt vmcnt(4)
	v_pk_fma_f32 v[22:23], v[22:23], v[178:179], v[182:183]
	v_pk_fma_f32 v[24:25], v[24:25], v[180:181], v[184:185]
	v_cvt_pk_bf16_f32 v22, v22, v23
	v_cvt_pk_bf16_f32 v23, v24, v25
	v_pk_add_f32 v[24:25], v[62:63], v[110:111] op_sel_hi:[1,0] neg_lo:[0,1] neg_hi:[0,1]
	v_pk_fma_f32 v[34:35], v[34:35], v[180:181], v[184:185]
	v_pk_mul_f32 v[24:25], v[24:25], v[112:113] op_sel_hi:[1,0]
	s_nop 0
	v_pk_fma_f32 v[24:25], v[24:25], v[178:179], v[182:183]
	s_nop 0
	v_cvt_pk_bf16_f32 v24, v24, v25
	v_cvt_pk_bf16_f32 v25, v34, v35
	ds_write2st64_b64 v149, v[22:23], v[24:25] offset1:64
	v_pk_add_f32 v[22:23], v[90:91], v[166:167] op_sel_hi:[1,0] neg_lo:[0,1] neg_hi:[0,1]
	v_pk_add_f32 v[24:25], v[92:93], v[166:167] op_sel_hi:[1,0] neg_lo:[0,1] neg_hi:[0,1]
	v_pk_mul_f32 v[22:23], v[22:23], v[168:169] op_sel_hi:[1,0]
	v_pk_mul_f32 v[24:25], v[24:25], v[168:169] op_sel_hi:[1,0]
	v_pk_fma_f32 v[22:23], v[22:23], v[178:179], v[182:183]
	v_pk_fma_f32 v[24:25], v[24:25], v[180:181], v[184:185]
	v_cvt_pk_bf16_f32 v22, v22, v23
	v_cvt_pk_bf16_f32 v23, v24, v25
	v_add_u32_e32 v24, 0x10000, v149
	ds_write_b64 v24, v[22:23]
	v_pk_add_f32 v[22:23], v[38:39], v[162:163] op_sel_hi:[1,0] neg_lo:[0,1] neg_hi:[0,1]
	v_pk_add_f32 v[24:25], v[40:41], v[162:163] op_sel_hi:[1,0] neg_lo:[0,1] neg_hi:[0,1]
	v_pk_mul_f32 v[22:23], v[22:23], v[164:165] op_sel_hi:[1,0]
	v_pk_mul_f32 v[24:25], v[24:25], v[164:165] op_sel_hi:[1,0]
	v_pk_fma_f32 v[22:23], v[22:23], v[178:179], v[182:183]
	v_pk_fma_f32 v[24:25], v[24:25], v[180:181], v[184:185]
	v_cvt_pk_bf16_f32 v22, v22, v23
	v_cvt_pk_bf16_f32 v23, v24, v25
	v_add_u32_e32 v24, 0x18000, v149
	v_ashrrev_i32_e32 v149, 31, v148
	ds_write_b64 v24, v[22:23]
	v_lshlrev_b64 v[22:23], 2, v[148:149]
	v_lshl_add_u64 v[24:25], s[10:11], 0, v[22:23]
	v_lshl_add_u64 v[26:27], s[18:19], 0, v[22:23]
	s_nop 0
	v_pk_add_f32 v[30:31], v[56:57], v[110:111] op_sel_hi:[1,0] neg_lo:[0,1] neg_hi:[0,1]
	s_waitcnt vmcnt(2)
	v_pk_fma_f32 v[6:7], v[6:7], v[186:187], v[190:191]
	v_pk_fma_f32 v[8:9], v[8:9], v[188:189], v[192:193]
	v_cvt_pk_bf16_f32 v6, v6, v7
	v_cvt_pk_bf16_f32 v7, v8, v9
	v_pk_add_f32 v[8:9], v[54:55], v[110:111] op_sel_hi:[1,0] neg_lo:[0,1] neg_hi:[0,1]
	v_pk_mul_f32 v[30:31], v[30:31], v[112:113] op_sel_hi:[1,0]
	v_pk_mul_f32 v[8:9], v[8:9], v[112:113] op_sel_hi:[1,0]
	v_pk_fma_f32 v[30:31], v[30:31], v[188:189], v[192:193]
	v_pk_fma_f32 v[8:9], v[8:9], v[186:187], v[190:191]
	s_nop 0
	v_cvt_pk_bf16_f32 v8, v8, v9
	v_cvt_pk_bf16_f32 v9, v30, v31
	ds_write2st64_b64 v147, v[6:7], v[8:9] offset1:64
	v_pk_add_f32 v[6:7], v[66:67], v[166:167] op_sel_hi:[1,0] neg_lo:[0,1] neg_hi:[0,1]
	v_pk_add_f32 v[8:9], v[68:69], v[166:167] op_sel_hi:[1,0] neg_lo:[0,1] neg_hi:[0,1]
	v_pk_mul_f32 v[6:7], v[6:7], v[168:169] op_sel_hi:[1,0]
	v_pk_mul_f32 v[8:9], v[8:9], v[168:169] op_sel_hi:[1,0]
	v_pk_fma_f32 v[6:7], v[6:7], v[186:187], v[190:191]
	v_pk_fma_f32 v[8:9], v[8:9], v[188:189], v[192:193]
	v_cvt_pk_bf16_f32 v6, v6, v7
	v_cvt_pk_bf16_f32 v7, v8, v9
	v_add_u32_e32 v8, 0x10000, v147
	ds_write_b64 v8, v[6:7]
	v_pk_add_f32 v[6:7], v[18:19], v[162:163] op_sel_hi:[1,0] neg_lo:[0,1] neg_hi:[0,1]
	v_pk_add_f32 v[8:9], v[20:21], v[162:163] op_sel_hi:[1,0] neg_lo:[0,1] neg_hi:[0,1]
	v_pk_mul_f32 v[6:7], v[6:7], v[164:165] op_sel_hi:[1,0]
	v_pk_mul_f32 v[8:9], v[8:9], v[164:165] op_sel_hi:[1,0]
	v_pk_fma_f32 v[6:7], v[6:7], v[186:187], v[190:191]
	v_pk_fma_f32 v[8:9], v[8:9], v[188:189], v[192:193]
	v_cvt_pk_bf16_f32 v6, v6, v7
	v_cvt_pk_bf16_f32 v7, v8, v9
	v_add_u32_e32 v8, 0x18000, v147
	v_ashrrev_i32_e32 v147, 31, v146
	ds_write_b64 v8, v[6:7]
	v_lshlrev_b64 v[6:7], 2, v[146:147]
	v_lshl_add_u64 v[8:9], s[10:11], 0, v[6:7]
	v_lshl_add_u64 v[18:19], s[18:19], 0, v[6:7]
	s_nop 0
	v_cmp_eq_u32_e64 s[10:11], 0, v212
	s_waitcnt vmcnt(0)
	v_pk_fma_f32 v[2:3], v[2:3], v[194:195], v[198:199]
	v_pk_fma_f32 v[4:5], v[4:5], v[196:197], v[200:201]
	v_cvt_pk_bf16_f32 v2, v2, v3
	v_cvt_pk_bf16_f32 v3, v4, v5
	v_pk_add_f32 v[4:5], v[14:15], v[110:111] op_sel_hi:[1,0] neg_lo:[0,1] neg_hi:[0,1]
	v_pk_add_f32 v[14:15], v[16:17], v[110:111] op_sel_hi:[1,0] neg_lo:[0,1] neg_hi:[0,1]
	v_pk_mul_f32 v[4:5], v[4:5], v[112:113] op_sel_hi:[1,0]
	v_pk_mul_f32 v[14:15], v[14:15], v[112:113] op_sel_hi:[1,0]
	v_pk_fma_f32 v[4:5], v[4:5], v[194:195], v[198:199]
	v_pk_fma_f32 v[14:15], v[14:15], v[196:197], v[200:201]
	v_cvt_pk_bf16_f32 v4, v4, v5
	v_cvt_pk_bf16_f32 v5, v14, v15
	ds_write2st64_b64 v165, v[2:3], v[4:5] offset1:64
	v_pk_add_f32 v[2:3], v[58:59], v[166:167] op_sel_hi:[1,0] neg_lo:[0,1] neg_hi:[0,1]
	v_pk_add_f32 v[4:5], v[60:61], v[166:167] op_sel_hi:[1,0] neg_lo:[0,1] neg_hi:[0,1]
	v_pk_mul_f32 v[2:3], v[2:3], v[168:169] op_sel_hi:[1,0]
	v_pk_mul_f32 v[4:5], v[4:5], v[168:169] op_sel_hi:[1,0]
	v_pk_fma_f32 v[2:3], v[2:3], v[194:195], v[198:199]
	v_pk_fma_f32 v[4:5], v[4:5], v[196:197], v[200:201]
	v_cvt_pk_bf16_f32 v2, v2, v3
	v_cvt_pk_bf16_f32 v3, v4, v5
	v_add_u32_e32 v4, 0x10000, v165
	ds_write_b64 v4, v[2:3]
	v_pk_add_f32 v[2:3], v[10:11], v[162:163] op_sel_hi:[1,0] neg_lo:[0,1] neg_hi:[0,1]
	v_pk_add_f32 v[4:5], v[12:13], v[162:163] op_sel_hi:[1,0] neg_lo:[0,1] neg_hi:[0,1]
	v_pk_mul_f32 v[2:3], v[2:3], v[164:165] op_sel_hi:[1,0]
	v_pk_mul_f32 v[4:5], v[4:5], v[164:165] op_sel_hi:[1,0]
	v_pk_fma_f32 v[2:3], v[2:3], v[194:195], v[198:199]
	v_pk_fma_f32 v[4:5], v[4:5], v[196:197], v[200:201]
	v_cvt_pk_bf16_f32 v2, v2, v3
	v_cvt_pk_bf16_f32 v3, v4, v5
	v_add_u32_e32 v4, 0x18000, v165
	ds_write_b64 v4, v[2:3]
	v_mov_b32_e32 v4, v229
	s_waitcnt lgkmcnt(0)
	s_barrier
	s_nop 0
	v_and_b32_e32 v5, 0x7f, v4
	v_ashrrev_i32_e32 v10, 7, v4
	v_bitop3_b32 v7, v10, v5, 15 bitop3:0x6c
	v_lshlrev_b32_e32 v6, 11, v10
	v_lshlrev_b32_e32 v7, 4, v7
	v_add3_u32 v6, 0, v6, v7
	ds_read_b128 v[6:9], v6
	v_lshlrev_b32_e32 v210, 4, v5
	v_ashrrev_i32_e32 v11, 31, v10
	v_lshl_add_u64 v[2:3], s[12:13], 0, v[210:211]
	v_lshlrev_b64 v[10:11], 11, v[10:11]
	v_lshl_add_u64 v[10:11], v[2:3], 0, v[10:11]
	s_waitcnt lgkmcnt(0)
	global_store_dwordx4 v[10:11], v[6:9], off
	s_lshl_b32 s12, s3, 8
	s_add_i32 s12, s5, s12
	v_add_u32_e32 v6, 0x200, v4
	v_ashrrev_i32_e32 v10, 7, v6
	v_bitop3_b32 v7, v10, v5, 15 bitop3:0x6c
	v_lshlrev_b32_e32 v6, 11, v10
	v_lshlrev_b32_e32 v7, 4, v7
	v_add3_u32 v6, 0, v6, v7
	ds_read_b128 v[6:9], v6
	v_ashrrev_i32_e32 v11, 31, v10
	v_lshlrev_b64 v[10:11], 11, v[10:11]
	v_lshl_add_u64 v[10:11], v[2:3], 0, v[10:11]
	s_lshr_b32 s5, s1, 20
	s_waitcnt lgkmcnt(0)
	global_store_dwordx4 v[10:11], v[6:9], off
	s_add_i32 s5, s0, s5
	s_and_b32 s5, s5, 0xfffff000
	v_add_u32_e32 v6, 0x400, v4
	v_ashrrev_i32_e32 v10, 7, v6
	v_bitop3_b32 v7, v10, v5, 15 bitop3:0x6c
	v_lshlrev_b32_e32 v6, 11, v10
	v_lshlrev_b32_e32 v7, 4, v7
	v_add3_u32 v6, 0, v6, v7
	ds_read_b128 v[6:9], v6
	v_ashrrev_i32_e32 v11, 31, v10
	v_lshlrev_b64 v[10:11], 11, v[10:11]
	v_lshl_add_u64 v[10:11], v[2:3], 0, v[10:11]
	s_sub_i32 s20, s0, s5
	s_waitcnt lgkmcnt(0)
	global_store_dwordx4 v[10:11], v[6:9], off
	s_ashr_i32 s13, s12, 31
	s_ashr_i32 s18, s20, 8
	v_add_u32_e32 v6, 0x600, v4
	v_ashrrev_i32_e32 v10, 7, v6
	v_bitop3_b32 v7, v10, v5, 15 bitop3:0x6c
	v_lshlrev_b32_e32 v6, 11, v10
	v_lshlrev_b32_e32 v7, 4, v7
	v_add3_u32 v6, 0, v6, v7
	ds_read_b128 v[6:9], v6
	v_ashrrev_i32_e32 v11, 31, v10
	v_lshlrev_b64 v[10:11], 11, v[10:11]
	v_lshl_add_u64 v[10:11], v[2:3], 0, v[10:11]
	s_ashr_i32 s19, s18, 31
	s_waitcnt lgkmcnt(0)
	global_store_dwordx4 v[10:11], v[6:9], off
	s_lshl_b64 s[12:13], s[12:13], 2
	s_nop 0
	v_add_u32_e32 v6, 0x800, v4
	v_ashrrev_i32_e32 v10, 7, v6
	v_bitop3_b32 v7, v10, v5, 15 bitop3:0x6c
	v_lshlrev_b32_e32 v6, 11, v10
	v_lshlrev_b32_e32 v7, 4, v7
	v_add3_u32 v6, 0, v6, v7
	ds_read_b128 v[6:9], v6
	v_ashrrev_i32_e32 v11, 31, v10
	v_lshlrev_b64 v[10:11], 11, v[10:11]
	v_lshl_add_u64 v[10:11], v[2:3], 0, v[10:11]
	s_waitcnt lgkmcnt(0)
	global_store_dwordx4 v[10:11], v[6:9], off
	s_nop 1
	v_add_u32_e32 v6, 0xa00, v4
	v_ashrrev_i32_e32 v10, 7, v6
	v_bitop3_b32 v7, v10, v5, 15 bitop3:0x6c
	v_lshlrev_b32_e32 v6, 11, v10
	v_lshlrev_b32_e32 v7, 4, v7
	v_add3_u32 v6, 0, v6, v7
	ds_read_b128 v[6:9], v6
	v_ashrrev_i32_e32 v11, 31, v10
	v_lshlrev_b64 v[10:11], 11, v[10:11]
	v_lshl_add_u64 v[10:11], v[2:3], 0, v[10:11]
	s_waitcnt lgkmcnt(0)
	global_store_dwordx4 v[10:11], v[6:9], off
	s_nop 1
	v_add_u32_e32 v6, 0xc00, v4
	v_ashrrev_i32_e32 v10, 7, v6
	v_bitop3_b32 v7, v10, v5, 15 bitop3:0x6c
	v_lshlrev_b32_e32 v6, 11, v10
	v_lshlrev_b32_e32 v7, 4, v7
	v_add3_u32 v6, 0, v6, v7
	ds_read_b128 v[6:9], v6
	v_ashrrev_i32_e32 v11, 31, v10
	v_lshlrev_b64 v[10:11], 11, v[10:11]
	v_lshl_add_u64 v[10:11], v[2:3], 0, v[10:11]
	s_waitcnt lgkmcnt(0)
	global_store_dwordx4 v[10:11], v[6:9], off
	s_nop 1
	v_add_u32_e32 v6, 0xe00, v4
	v_ashrrev_i32_e32 v10, 7, v6
	v_bitop3_b32 v7, v10, v5, 15 bitop3:0x6c
	v_lshlrev_b32_e32 v6, 11, v10
	v_lshlrev_b32_e32 v7, 4, v7
	v_add3_u32 v6, 0, v6, v7
	ds_read_b128 v[6:9], v6
	v_ashrrev_i32_e32 v11, 31, v10
	v_lshlrev_b64 v[10:11], 11, v[10:11]
	v_lshl_add_u64 v[10:11], v[2:3], 0, v[10:11]
	s_waitcnt lgkmcnt(0)
	global_store_dwordx4 v[10:11], v[6:9], off
	s_nop 1
	v_add_u32_e32 v6, 0x1000, v4
	v_ashrrev_i32_e32 v10, 7, v6
	v_bitop3_b32 v7, v10, v5, 15 bitop3:0x6c
	v_lshlrev_b32_e32 v6, 11, v10
	v_lshlrev_b32_e32 v7, 4, v7
	v_add3_u32 v6, 0, v6, v7
	ds_read_b128 v[6:9], v6
	v_ashrrev_i32_e32 v11, 31, v10
	v_lshlrev_b64 v[10:11], 11, v[10:11]
	v_lshl_add_u64 v[10:11], v[2:3], 0, v[10:11]
	s_waitcnt lgkmcnt(0)
	global_store_dwordx4 v[10:11], v[6:9], off
	s_nop 1
	v_add_u32_e32 v6, 0x1200, v4
	v_ashrrev_i32_e32 v10, 7, v6
	v_bitop3_b32 v7, v10, v5, 15 bitop3:0x6c
	v_lshlrev_b32_e32 v6, 11, v10
	v_lshlrev_b32_e32 v7, 4, v7
	v_add3_u32 v6, 0, v6, v7
	ds_read_b128 v[6:9], v6
	v_ashrrev_i32_e32 v11, 31, v10
	v_lshlrev_b64 v[10:11], 11, v[10:11]
	v_lshl_add_u64 v[10:11], v[2:3], 0, v[10:11]
	s_waitcnt lgkmcnt(0)
	global_store_dwordx4 v[10:11], v[6:9], off
	s_nop 1
	v_add_u32_e32 v6, 0x1400, v4
	v_ashrrev_i32_e32 v10, 7, v6
	v_bitop3_b32 v7, v10, v5, 15 bitop3:0x6c
	v_lshlrev_b32_e32 v6, 11, v10
	v_lshlrev_b32_e32 v7, 4, v7
	v_add3_u32 v6, 0, v6, v7
	ds_read_b128 v[6:9], v6
	v_ashrrev_i32_e32 v11, 31, v10
	v_lshlrev_b64 v[10:11], 11, v[10:11]
	v_lshl_add_u64 v[10:11], v[2:3], 0, v[10:11]
	s_waitcnt lgkmcnt(0)
	global_store_dwordx4 v[10:11], v[6:9], off
	s_nop 1
	v_add_u32_e32 v6, 0x1600, v4
	v_ashrrev_i32_e32 v10, 7, v6
	v_bitop3_b32 v7, v10, v5, 15 bitop3:0x6c
	v_lshlrev_b32_e32 v6, 11, v10
	v_lshlrev_b32_e32 v7, 4, v7
	v_add3_u32 v6, 0, v6, v7
	ds_read_b128 v[6:9], v6
	v_ashrrev_i32_e32 v11, 31, v10
	v_lshlrev_b64 v[10:11], 11, v[10:11]
	v_lshl_add_u64 v[10:11], v[2:3], 0, v[10:11]
	s_waitcnt lgkmcnt(0)
	global_store_dwordx4 v[10:11], v[6:9], off
	s_nop 1
	v_add_u32_e32 v6, 0x1800, v4
	v_ashrrev_i32_e32 v10, 7, v6
	v_bitop3_b32 v7, v10, v5, 15 bitop3:0x6c
	v_lshlrev_b32_e32 v6, 11, v10
	v_lshlrev_b32_e32 v7, 4, v7
	v_add3_u32 v6, 0, v6, v7
	ds_read_b128 v[6:9], v6
	v_ashrrev_i32_e32 v11, 31, v10
	v_lshlrev_b64 v[10:11], 11, v[10:11]
	v_lshl_add_u64 v[10:11], v[2:3], 0, v[10:11]
	s_waitcnt lgkmcnt(0)
	global_store_dwordx4 v[10:11], v[6:9], off
	s_nop 1
	v_add_u32_e32 v6, 0x1a00, v4
	v_ashrrev_i32_e32 v10, 7, v6
	v_bitop3_b32 v7, v10, v5, 15 bitop3:0x6c
	v_lshlrev_b32_e32 v6, 11, v10
	v_lshlrev_b32_e32 v7, 4, v7
	v_add3_u32 v6, 0, v6, v7
	ds_read_b128 v[6:9], v6
	v_ashrrev_i32_e32 v11, 31, v10
	v_lshlrev_b64 v[10:11], 11, v[10:11]
	v_lshl_add_u64 v[10:11], v[2:3], 0, v[10:11]
	s_waitcnt lgkmcnt(0)
	global_store_dwordx4 v[10:11], v[6:9], off
	s_nop 1
	v_add_u32_e32 v6, 0x1c00, v4
	v_ashrrev_i32_e32 v10, 7, v6
	v_bitop3_b32 v7, v10, v5, 15 bitop3:0x6c
	v_lshlrev_b32_e32 v6, 11, v10
	v_lshlrev_b32_e32 v7, 4, v7
	v_add3_u32 v6, 0, v6, v7
	ds_read_b128 v[6:9], v6
	v_ashrrev_i32_e32 v11, 31, v10
	v_lshlrev_b64 v[10:11], 11, v[10:11]
	v_lshl_add_u64 v[10:11], v[2:3], 0, v[10:11]
	v_add_u32_e32 v4, 0x1e00, v4
	s_waitcnt lgkmcnt(0)
	global_store_dwordx4 v[10:11], v[6:9], off
	s_nop 1
	v_ashrrev_i32_e32 v8, 7, v4
	v_bitop3_b32 v5, v8, v5, 15 bitop3:0x6c
	v_lshlrev_b32_e32 v4, 11, v8
	v_lshlrev_b32_e32 v5, 4, v5
	v_add3_u32 v4, 0, v4, v5
	ds_read_b128 v[4:7], v4
	v_ashrrev_i32_e32 v9, 31, v8
	v_lshlrev_b64 v[8:9], 11, v[8:9]
	v_lshl_add_u64 v[2:3], v[2:3], 0, v[8:9]
	s_waitcnt lgkmcnt(0)
	global_store_dwordx4 v[2:3], v[4:7], off
	s_load_dwordx4 s[88:91], s[14:15], 0x90
	v_xor_b32_e32 v2, 1, v223
	v_cmp_lt_i32_e32 vcc, v2, v109
	s_waitcnt lgkmcnt(0)
	s_add_u32 s3, s90, s12
	v_cndmask_b32_e32 v2, v223, v2, vcc
	s_addc_u32 s5, s91, s13
	s_lshl_b64 s[12:13], s[18:19], 2
	v_lshlrev_b32_e32 v238, 2, v2
	v_xor_b32_e32 v2, 2, v223
	s_add_u32 s15, s3, s12
	v_cmp_lt_i32_e32 vcc, v2, v109
	s_addc_u32 s71, s5, s13
	s_add_u32 s72, s15, 64
	v_cndmask_b32_e32 v2, v223, v2, vcc
	v_lshlrev_b32_e32 v239, 2, v2
	v_xor_b32_e32 v2, 4, v223
	s_addc_u32 s74, s71, 0
	s_lshl_b64 s[12:13], s[84:85], 2
	v_cmp_lt_i32_e32 vcc, v2, v109
	s_add_u32 s3, s88, s12
	s_addc_u32 s5, s89, s13
	v_cndmask_b32_e32 v2, v223, v2, vcc
	s_lshl_b64 s[12:13], s[82:83], 2
	v_lshlrev_b32_e32 v240, 2, v2
	v_xor_b32_e32 v2, 8, v223
	s_add_u32 s83, s3, s12
	v_cmp_lt_i32_e32 vcc, v2, v109
	s_addc_u32 s85, s5, s13
	s_add_u32 s42, s83, 4
	v_cndmask_b32_e32 v2, v223, v2, vcc
	v_lshlrev_b32_e32 v241, 2, v2
	s_addc_u32 s43, s85, 0
	s_or_b32 s64, s0, 16
	s_or_b32 s65, s0, 32
	s_or_b32 s70, s0, 48
	s_lshl_b64 s[16:17], s[16:17], 1
	s_branch .LBB0_506

.LBB0_626:
	v_mov_b32_e32 v36, v0
	v_cmp_lt_i32_e32 vcc, v184, v185
	v_and_b32_e32 v192, 63, v36
	v_or_b32_e32 v4, s59, v192
	v_ashrrev_i32_e32 v5, 31, v4
	v_lshl_add_u64 v[4:5], v[4:5], 2, s[18:19]
	global_load_dword v4, v[4:5], off
	s_add_i32 s98, s48, s60
	s_ashr_i32 s99, s98, 31
	s_lshl_b64 s[98:99], s[98:99], 2
	s_add_u32 s98, s38, s98
	s_addc_u32 s99, s39, s99
	v_mov_b32_e32 v252, 0
	v_mov_b32_e32 v253, 0
	global_load_dword v252, v252, s[98:99]
	global_load_dword v253, v253, s[40:41]
	v_cndmask_b32_e32 v2, v184, v183, vcc
	v_lshlrev_b32_e32 v2, 2, v2
	v_cmp_lt_i32_e32 vcc, v186, v185
	v_cmp_gt_u32_e64 s[10:11], 32, v192
	s_lshl_b32 s49, s48, 8
	v_cndmask_b32_e32 v5, v186, v183, vcc
	v_cmp_eq_u32_e32 vcc, 0, v192
	v_lshlrev_b32_e32 v5, 2, v5
	v_ashrrev_i32_e32 v37, 31, v36
	s_mov_b32 s2, 0
	s_add_i32 s14, s49, 0x100
	s_waitcnt vmcnt(0)
	ds_bpermute_b32 v2, v2, v4
	s_waitcnt lgkmcnt(0)
	v_add_f32_e32 v2, v4, v2
	v_cndmask_b32_e32 v2, v2, v4, vcc
	ds_bpermute_b32 v5, v5, v2
	v_cmp_lt_i32_e32 vcc, v187, v185
	s_waitcnt lgkmcnt(0)
	v_add_f32_e32 v5, v2, v5
	v_cndmask_b32_e32 v6, v187, v183, vcc
	v_cmp_gt_u32_e32 vcc, 2, v192
	v_lshlrev_b32_e32 v6, 2, v6
	s_nop 0
	v_cndmask_b32_e32 v2, v5, v2, vcc
	ds_bpermute_b32 v5, v6, v2
	v_cmp_lt_i32_e32 vcc, v188, v185
	s_waitcnt lgkmcnt(0)
	v_add_f32_e32 v5, v2, v5
	v_cndmask_b32_e32 v6, v188, v183, vcc
	v_cmp_gt_u32_e32 vcc, 4, v192
	v_lshlrev_b32_e32 v6, 2, v6
	s_nop 0
	v_cndmask_b32_e32 v2, v5, v2, vcc
	ds_bpermute_b32 v5, v6, v2
	v_cmp_lt_i32_e32 vcc, v189, v185
	s_waitcnt lgkmcnt(0)
	v_add_f32_e32 v5, v2, v5
	v_cndmask_b32_e32 v6, v189, v183, vcc
	v_cmp_gt_u32_e32 vcc, 8, v192
	v_lshlrev_b32_e32 v6, 2, v6
	s_nop 0
	v_cndmask_b32_e32 v2, v5, v2, vcc
	ds_bpermute_b32 v5, v6, v2
	v_cmp_lt_i32_e32 vcc, v190, v185
	s_waitcnt lgkmcnt(0)
	v_add_f32_e32 v5, v2, v5
	v_cndmask_b32_e32 v6, v190, v183, vcc
	v_cmp_gt_u32_e32 vcc, 16, v192
	v_lshlrev_b32_e32 v6, 2, v6
	s_nop 0
	v_cndmask_b32_e32 v5, v5, v2, vcc
	ds_bpermute_b32 v6, v6, v5
	v_lshl_add_u32 v2, v36, 2, s33
	s_waitcnt lgkmcnt(0)
	v_add_f32_e32 v6, v5, v6
	v_cndmask_b32_e64 v5, v6, v5, s[10:11]
	v_sub_f32_e32 v6, v5, v4
	v_lshl_add_u64 v[4:5], v[36:37], 2, s[42:43]
	v_lshlrev_b32_e32 v8, 2, v36
	v_lshrrev_b32_e32 v12, 6, v36
	global_load_dword v16, v8, s[42:43]
	global_load_dword v17, v8, s[42:43] offset:2048
	v_add_u32_e32 v9, 0x1000, v8
	v_add_u32_e32 v10, 0x2000, v8
	global_load_dword v18, v9, s[42:43]
	global_load_dword v19, v9, s[42:43] offset:2048
	v_add_u32_e32 v11, 0x3000, v8
	global_load_dword v20, v10, s[42:43]
	global_load_dword v21, v10, s[42:43] offset:2048
	global_load_dword v22, v11, s[42:43]
	global_load_dword v23, v11, s[42:43] offset:2048
	v_add_u32_e32 v13, 0, v12
	v_or_b32_e32 v13, v13, v185
	v_lshlrev_b32_e32 v13, 2, v13
	ds_bpermute_b32 v24, v13, v6
	v_add_u32_e32 v14, 8, v12
	v_or_b32_e32 v14, v14, v185
	v_lshlrev_b32_e32 v14, 2, v14
	ds_bpermute_b32 v25, v14, v6
	v_add_u32_e32 v15, 16, v12
	v_or_b32_e32 v15, v15, v185
	v_lshlrev_b32_e32 v15, 2, v15
	ds_bpermute_b32 v26, v15, v6
	v_add_u32_e32 v32, 24, v12
	v_or_b32_e32 v32, v32, v185
	v_lshlrev_b32_e32 v32, 2, v32
	ds_bpermute_b32 v27, v32, v6
	v_add_u32_e32 v33, 32, v12
	v_or_b32_e32 v33, v33, v185
	v_lshlrev_b32_e32 v33, 2, v33
	ds_bpermute_b32 v28, v33, v6
	v_add_u32_e32 v34, 40, v12
	v_or_b32_e32 v34, v34, v185
	v_lshlrev_b32_e32 v34, 2, v34
	ds_bpermute_b32 v29, v34, v6
	v_add_u32_e32 v35, 48, v12
	v_or_b32_e32 v35, v35, v185
	v_lshlrev_b32_e32 v35, 2, v35
	ds_bpermute_b32 v30, v35, v6
	v_add_u32_e32 v4, 56, v12
	v_or_b32_e32 v4, v4, v185
	v_lshlrev_b32_e32 v4, 2, v4
	ds_bpermute_b32 v31, v4, v6
	s_waitcnt vmcnt(0) lgkmcnt(0)
	v_add_f32_e32 v16, v16, v24
	v_mul_f32_e32 v16, 0x3fb8aa3b, v16
	ds_write_b32 v2, v16
	v_add_f32_e32 v17, v17, v25
	v_mul_f32_e32 v17, 0x3fb8aa3b, v17
	ds_write_b32 v2, v17 offset:2048
	v_add_f32_e32 v18, v18, v26
	v_mul_f32_e32 v18, 0x3fb8aa3b, v18
	ds_write_b32 v2, v18 offset:4096
	v_add_f32_e32 v19, v19, v27
	v_mul_f32_e32 v19, 0x3fb8aa3b, v19
	ds_write_b32 v2, v19 offset:6144
	v_add_f32_e32 v20, v20, v28
	v_mul_f32_e32 v20, 0x3fb8aa3b, v20
	ds_write_b32 v2, v20 offset:8192
	v_add_f32_e32 v21, v21, v29
	v_mul_f32_e32 v21, 0x3fb8aa3b, v21
	ds_write_b32 v2, v21 offset:10240
	v_add_f32_e32 v22, v22, v30
	v_mul_f32_e32 v22, 0x3fb8aa3b, v22
	ds_write_b32 v2, v22 offset:12288
	v_add_f32_e32 v23, v23, v31
	v_mul_f32_e32 v23, 0x3fb8aa3b, v23
	ds_write_b32 v2, v23 offset:14336
.LBB0_630:
	s_lshl_b32 s12, s49, 2
	s_add_i32 s45, s12, 0
	s_add_i32 s45, s45, 0x14800
	s_lshr_b32 s46, s14, 6
	v_readfirstlane_b32 s2, v36
	s_cmp_eq_u32 s48, 0
	s_mov_b32 s12, 0
	s_waitcnt lgkmcnt(0)
	s_barrier
	s_cbranch_scc1 .LBB0_634
	s_add_i32 s12, s48, s60
	s_ashr_i32 s13, s12, 31
	s_lshl_b64 s[12:13], s[12:13], 2
	s_add_u32 s12, s38, s12
	s_addc_u32 s13, s39, s13
	v_mov_b32_e32 v2, v252
	v_mov_b32_e32 v4, v253
	v_mov_b32_e32 v5, s45
	ds_read_b32 v5, v5
	s_mov_b32 s47, 0x3f828f5c
	s_add_i32 s44, s46, -4
	s_waitcnt vmcnt(1)
	v_mul_f32_e32 v6, 0x4f800000, v2
	v_cmp_gt_f32_e32 vcc, s52, v2
	s_waitcnt vmcnt(0)
	v_mul_f32_e32 v7, 0x4f800000, v4
	v_cmp_gt_f32_e64 s[12:13], s52, v4
	v_cndmask_b32_e32 v2, v2, v6, vcc
	v_sqrt_f32_e32 v6, v2
	v_cndmask_b32_e64 v4, v4, v7, s[12:13]
	v_sqrt_f32_e32 v7, v4
	v_add_u32_e32 v8, -1, v6
	v_fma_f32 v12, -v8, v6, v2
	v_add_u32_e32 v10, -1, v7
	v_add_u32_e32 v9, 1, v6
	v_fma_f32 v14, -v10, v7, v4
	v_cmp_ge_f32_e64 s[14:15], 0, v12
	v_add_u32_e32 v11, 1, v7
	v_fma_f32 v13, -v9, v6, v2
	v_cndmask_b32_e64 v6, v6, v8, s[14:15]
	v_cmp_ge_f32_e64 s[14:15], 0, v14
	v_fma_f32 v15, -v11, v7, v4
	s_nop 0
	v_cndmask_b32_e64 v7, v7, v10, s[14:15]
	v_cmp_lt_f32_e64 s[14:15], 0, v13
	s_nop 1
	v_cndmask_b32_e64 v6, v6, v9, s[14:15]
	v_cmp_lt_f32_e64 s[14:15], 0, v15
	v_mul_f32_e32 v8, 0x37800000, v6
	v_cndmask_b32_e32 v6, v6, v8, vcc
	v_cndmask_b32_e64 v7, v7, v11, s[14:15]
	v_mul_f32_e32 v9, 0x37800000, v7
	v_cmp_class_f32_e32 vcc, v2, v182
	v_cndmask_b32_e64 v7, v7, v9, s[12:13]
	s_mov_b32 s12, 0
	v_cndmask_b32_e32 v2, v6, v2, vcc
	v_cmp_class_f32_e32 vcc, v4, v182
	s_nop 1
	v_cndmask_b32_e32 v4, v7, v4, vcc
	v_mul_f32_e32 v2, v2, v4
	v_fma_f32 v2, v2, s47, 1.0
	v_sub_f32_e32 v2, 0xc3160000, v2
	s_waitcnt lgkmcnt(0)
	v_sub_f32_e32 v2, v2, v5
